# speedup vs baseline: 1.0142x; 1.0142x over previous
_Z16bilateral_kernelPKfS0_Pf:
	s_load_dwordx2 s[4:5], s[0:1], 0x0
	s_load_dwordx2 s[8:9], s[0:1], 0x10
	s_lshr_b32 s19, s2, 8
	s_and_b32 s0, s2, 7
	s_mulk_i32 s0, 0x60
	s_lshr_b32 s1, s2, 3
	s_add_i32 s1, s0, s1
	s_lshr_b32 s0, s1, 6
	s_lshl_b32 s11, s1, 6
	s_nop 0
	s_and_b32 s11, s11, 0x1c0
	s_lshl_b32 s1, s1, 3
	s_nop 0
	s_and_b32 s10, s1, 0x1c0
	s_mov_b32 s1, 0
	s_lshl_b64 s[2:3], s[0:1], 20
	s_mov_b32 s20, 0xc05dfbe6
	s_mov_b32 s21, 0xc05dfbe6
	s_mov_b32 s22, 0xc0a8390e
	s_mov_b32 s23, 0xc0a8390e
	s_mov_b32 s24, 0xc08211a7
	s_mov_b32 s25, 0xc08211a7
	s_mov_b32 s26, 0xc0bb4cc1
	s_mov_b32 s27, 0xc0bb4cc1
	s_mov_b32 s28, 0xc0f487dc
	s_mov_b32 s29, 0xc0f487dc
	s_mov_b32 s30, 0x3e0bd796
	s_mov_b32 s31, 0x3e0bd796
	s_mov_b32 s32, 0x3f45a90c
	s_mov_b32 s33, 0x3f45a90c
	s_mov_b32 s34, 0x3fa5c782
	s_mov_b32 s35, 0x3fa5c782
	v_and_b32_e32 v118, 15, v0
	v_lshrrev_b32_e32 v115, 2, v0
	v_lshl_or_b32 v113, v118, 2, s11
	v_and_or_b32 v117, v115, 60, s10
	v_min_u32_e32 v116, 0x1fa, v113
	v_sub_u32_e64 v115, v113, 2 clamp
	v_add_u32_e64 v116, 4, v116
	v_cmp_eq_u32_e64 s[16:17], 0, v118
	v_cmp_eq_u32_e32 vcc, 15, v118
	s_nop 1
	v_cndmask_b32_e64 v115, v116, v115, s[16:17]
	s_or_b64 vcc, s[16:17], vcc
	v_lshlrev_b32_e32 v115, 2, v115
	v_mov_b32_e32 v116, 0x7ff00000
	s_nop 0
	v_cndmask_b32_e32 v112, v116, v115, vcc
	s_movk_i32 s18, 0x1fc
	v_cmp_eq_u32_e32 vcc, 0, v113
	v_cmp_eq_u32_e64 s[16:17], s18, v113
	v_lshlrev_b32_e32 v113, 2, v113
	s_waitcnt lgkmcnt(0)
	s_add_u32 s4, s4, s2
	s_addc_u32 s5, s5, s3
	s_and_b32 s5, s5, 0xffff
	s_mov_b32 s6, 0x100000
	s_mov_b32 s7, 0x20000
	s_add_u32 s12, s8, s2
	s_addc_u32 s13, s9, s3
	s_and_b32 s13, s13, 0xffff
	s_mov_b32 s14, 0x100000
	s_mov_b32 s15, 0x20000
	v_sub_u32_e64 v115, v117, 2 clamp
	v_lshlrev_b32_e32 v115, 11, v115
	v_add_u32_e32 v116, v115, v112
	v_add_u32_e64 v115, v115, v113
	buffer_load_dwordx2 v[0:1], v116, s[4:7], 0 offen nt
	buffer_load_dwordx2 v[6:7], v116, s[4:7], 0 offen nt
	buffer_load_dwordx4 v[2:5], v115, s[4:7], 0 offen nt
	v_sub_u32_e64 v115, v117, 1 clamp
	v_lshlrev_b32_e32 v115, 11, v115
	v_add_u32_e32 v116, v115, v112
	v_add_u32_e64 v115, v115, v113
	buffer_load_dwordx2 v[8:9], v116, s[4:7], 0 offen nt
	buffer_load_dwordx2 v[14:15], v116, s[4:7], 0 offen nt
	buffer_load_dwordx4 v[10:13], v115, s[4:7], 0 offen nt
	v_lshlrev_b32_e32 v115, 11, v117
	v_add_u32_e32 v124, v115, v112
	v_add_u32_e32 v125, v115, v113
	v_mov_b32_e32 v114, v125
	v_add_u32_e32 v119, 0x1000, v114
	buffer_load_dwordx2 v[16:17], v124, s[4:7], 0 offen nt
	buffer_load_dwordx2 v[22:23], v124, s[4:7], 0 offen nt
	buffer_load_dwordx4 v[18:21], v125, s[4:7], 0 offen nt
	buffer_load_dwordx2 v[24:25], v124, s[4:7], 0 offen offset:2048 nt
	buffer_load_dwordx2 v[30:31], v124, s[4:7], 0 offen offset:2048 nt
	buffer_load_dwordx4 v[26:29], v125, s[4:7], 0 offen offset:2048 nt
	v_lshlrev_b32_e64 v115, 11, v117
	v_add_u32_e32 v115, 0x1000, v115
	v_add_u32_e32 v124, v115, v112
	v_add_u32_e32 v125, v115, v113
	buffer_load_dwordx2 v[32:33], v124, s[4:7], 0 offen nt
	buffer_load_dwordx2 v[38:39], v124, s[4:7], 0 offen nt
	buffer_load_dwordx4 v[34:37], v125, s[4:7], 0 offen nt
	buffer_load_dwordx2 v[40:41], v124, s[4:7], 0 offen offset:2048 nt
	buffer_load_dwordx2 v[46:47], v124, s[4:7], 0 offen offset:2048 nt
	buffer_load_dwordx4 v[42:45], v125, s[4:7], 0 offen offset:2048 nt
	v_min_u32_e32 v115, 0x1fb, v117
	v_lshlrev_b32_e64 v115, 11, v115
	v_add_u32_e32 v115, 0x2000, v115
	v_add_u32_e32 v116, v115, v112
	v_add_u32_e32 v115, v115, v113
	buffer_load_dwordx2 v[48:49], v116, s[4:7], 0 offen nt
	buffer_load_dwordx2 v[54:55], v116, s[4:7], 0 offen nt
	buffer_load_dwordx4 v[50:53], v115, s[4:7], 0 offen nt
	v_min_u32_e32 v115, 0x1fa, v117
	v_lshlrev_b32_e64 v115, 11, v115
	v_add_u32_e32 v115, 0x2800, v115
	v_add_u32_e32 v116, v115, v112
	v_add_u32_e32 v115, v115, v113
	buffer_load_dwordx2 v[56:57], v116, s[4:7], 0 offen nt
	buffer_load_dwordx2 v[62:63], v116, s[4:7], 0 offen nt
	buffer_load_dwordx4 v[58:61], v115, s[4:7], 0 offen nt
	s_cmp_eq_u32 s19, 0
	s_cbranch_scc1 .Lmyp0
	s_cmp_eq_u32 s19, 1
	s_cbranch_scc1 .Lmyp1
	s_setprio 0
	s_branch .Lmypd
